# grid barrier: flat cross-XCD level - XCD leaders add to per-XCD flag words in one 64B line, all workgroups poll that line (sum of flags); the returning cross-XCD arrival atomic and the generation word
# baseline (speedup 1.0000x reference)
; __device__ __forceinline__ int tid_from_wave(int wave) { unsigned l_; asm volatile("v_mbcnt_lo_u32_b32 %0, -1, 0\n\tv_mbcnt_hi_u32_b32 %0, -1, %0" : "=v"(l_)); return wave * 64 + (int)l_; }
; #define LAS __attribute__((address_space(3)))
; __device__ __forceinline__ unsigned xb_add(unsigned* p, unsigned v) { return __hip_atomic_fetch_add(p, v, __ATOMIC_RELAXED, __HIP_MEMORY_SCOPE_AGENT); }
; __device__ __forceinline__ unsigned xb_xcc_id() { return (unsigned)__builtin_amdgcn_s_getreg((3 << 11) | 20) & 0xFu; }
; __device__ __forceinline__ XcdBarrier xcd_barrier_post(unsigned* bar, volatile LAS unsigned* st, int wave) {
;     XcdBarrier b; b.bar = bar; b.x = xb_xcc_id(); b.st = st; b.wave = wave;
;     if (tid_from_wave(wave) == 0) (void)xb_add(&bar[XB_XCNT(b.x)], 1u);
;     return b;
; }
; __global__ void __launch_bounds__(NWAVES * 64, 2) fwd(Args args) {
;     extern __shared__ __attribute__((aligned(16))) unsigned char lds_raw[];
;     ...
;     LAS unsigned char* const lds0 = (LAS unsigned char*)lds_raw;
;     const int wave_s = __builtin_amdgcn_readfirstlane((int)(threadIdx.x >> 6));
;     unsigned char* ws = args.ws; const In& I = args.in;
;     unsigned* ctl = (unsigned*)(ws + WS_CTL);
;     for (int u = threadIdx.x; u < (LDS_BYTES - LDSCTL_OFF) / 4; u += NWAVES * 64) ((LAS unsigned*)(lds0 + LDSCTL_OFF))[u] = 0u;
;     __syncthreads();
;     XcdBarrier bar; bar.bar = ctl + CW_BAR; bar.x = 0; bar.st = nullptr; bar.wave = wave_s;
;     if (!MK_PER_PHASE) bar = xcd_barrier_post(ctl + CW_BAR, (volatile LAS unsigned*)(lds0 + MISC_OFF) + 8, wave_s);
_Z3fwd4Args:
	s_mov_b32 s98, 0
	s_mov_b32 s33, s2
	v_writelane_b32 v254, s0, 0
	s_load_dwordx8 s[88:95], s[0:1], 0x100
	v_readfirstlane_b32 s4, v0
	v_writelane_b32 v254, s1, 1
	s_movk_i32 s0, 0x100
	v_cmp_gt_u32_e32 vcc, s0, v0
	s_and_saveexec_b64 s[0:1], vcc
	v_lshl_add_u32 v0, v0, 2, 0
	v_add_u32_e32 v0, 0x23c00, v0
	v_mov_b32_e32 v1, 0
	ds_write_b32 v0, v1
	s_or_b64 exec, exec, s[0:1]
	v_readlane_b32 s0, v254, 0
	v_readlane_b32 s1, v254, 1
	s_load_dwordx16 s[56:71], s[0:1], 0x0
	s_load_dwordx16 s[72:87], s[0:1], 0x40
	s_load_dwordx16 s[8:23], s[0:1], 0x80
	s_waitcnt lgkmcnt(0)
	s_add_u32 s0, s92, 0x4000
	s_addc_u32 s1, s93, 0
	s_barrier
	v_writelane_b32 v254, s8, 2
	s_and_b32 s96, s4, 0xffffffc0
	s_nop 0
	v_writelane_b32 v254, s9, 3
	v_writelane_b32 v254, s10, 4
	v_writelane_b32 v254, s11, 5
	v_writelane_b32 v254, s12, 6
	v_writelane_b32 v254, s13, 7
	v_writelane_b32 v254, s14, 8
	v_writelane_b32 v254, s15, 9
	v_writelane_b32 v254, s16, 10
	v_writelane_b32 v254, s17, 11
	v_writelane_b32 v254, s18, 12
	v_writelane_b32 v254, s19, 13
	v_writelane_b32 v254, s20, 14
	v_writelane_b32 v254, s21, 15
	v_writelane_b32 v254, s22, 16
	v_writelane_b32 v254, s23, 17
	v_writelane_b32 v254, s0, 18
	s_nop 1
	v_writelane_b32 v254, s1, 19
	s_getreg_b32 s0, hwreg(HW_REG_XCC_ID, 0, 4)
	s_and_b32 s97, s0, 15
	s_sub_i32 s0, 0, s96
	v_mbcnt_lo_u32_b32 v0, -1, 0
	v_mbcnt_hi_u32_b32 v0, -1, v0
	v_writelane_b32 v254, s4, 20
	v_cmp_eq_u32_e32 vcc, s0, v0
	v_writelane_b32 v254, s0, 21
	s_and_saveexec_b64 s[0:1], vcc
	s_cbranch_execz .LBB0_5
	s_mov_b64 s[2:3], exec
	v_mbcnt_lo_u32_b32 v0, s2, 0
	v_mbcnt_hi_u32_b32 v0, s3, v0
	v_cmp_eq_u32_e32 vcc, 0, v0
	s_and_b64 s[4:5], exec, vcc
	s_mov_b64 exec, s[4:5]
	s_cbranch_execz .LBB0_5
	s_bcnt1_i32_b64 s2, s[2:3]
	s_lshl_b32 s4, s97, 8
	v_mov_b32_e32 v1, s2
	v_readlane_b32 s2, v254, 18
	v_mov_b32_e32 v0, s4
	v_readlane_b32 s3, v254, 19
	s_nop 4
	global_atomic_add v0, v1, s[2:3] offset:1024

; __device__ __forceinline__ int tid_from_wave(int wave) { unsigned l_; asm volatile("v_mbcnt_lo_u32_b32 %0, -1, 0\n\tv_mbcnt_hi_u32_b32 %0, -1, %0" : "=v"(l_)); return wave * 64 + (int)l_; }
; __device__ __forceinline__ unsigned xb_ld(unsigned* p)              { return __hip_atomic_load(p, __ATOMIC_RELAXED, __HIP_MEMORY_SCOPE_AGENT); }
; __device__ __forceinline__ unsigned xb_add(unsigned* p, unsigned v) { return __hip_atomic_fetch_add(p, v, __ATOMIC_RELAXED, __HIP_MEMORY_SCOPE_AGENT); }
; #define XB_SPIN(cond, bar) do { unsigned _sp = 0; while (cond) { __builtin_amdgcn_s_sleep(1); \
;     if ((++_sp & 255u) == 0u) { if (xb_ld(&(bar)[XB_TMO])) break; if (_sp > XB_SPIN_CAP) { atomicAdd(&(bar)[XB_TMO], 1u); break; } } } } while (0)
; __device__ __forceinline__ void xcd_barrier(const XcdBarrier& b) {
;     asm volatile("s_waitcnt vmcnt(0)" ::: "memory");
;     __syncthreads();
;     if (tid_from_wave(b.wave) == 0) {
;         unsigned* bar = b.bar;
;         __builtin_amdgcn_s_waitcnt(0);
;         unsigned nloc = b.st[0], nx = b.st[1];
;         if (nloc == 0u) { xcd_barrier_complete(bar, b.x, nloc, nx); b.st[0] = nloc; b.st[1] = nx; }
;         const unsigned old = xb_add(&bar[XB_XSUB(b.x)], 1u);
;         const unsigned gen = old / nloc;
;         if (old + 1u == (gen + 1u) * nloc) {
;             __builtin_amdgcn_fence(__ATOMIC_RELEASE, "agent");
;             asm volatile("s_waitcnt vmcnt(0)" ::: "memory");
;             const unsigned og = xb_add(&bar[XB_TOP], 1u);
;             const unsigned tg = og / nx;
;             if (og + 1u == (tg + 1u) * nx) xb_add(&bar[XB_TOPGEN], 1u);
;             else XB_SPIN(xb_ld(&bar[XB_TOPGEN]) == tg, bar);
;             __builtin_amdgcn_fence(__ATOMIC_ACQUIRE, "agent");
;             xb_add(&bar[XB_XGEN(b.x)], 1u);
;             asm volatile("s_waitcnt vmcnt(0)" ::: "memory");
;         } else {
;             XB_SPIN(xb_ld(&bar[XB_XGEN(b.x)]) == gen, bar);
;             __builtin_amdgcn_fence(__ATOMIC_ACQUIRE, "agent");
;             asm volatile("s_waitcnt vmcnt(0)" ::: "memory");
;         }
;     }
;     __syncthreads();
; }
.LBB0_121:
	s_waitcnt lgkmcnt(0)
	v_readfirstlane_b32 s14, v2
	v_readfirstlane_b32 s15, v0
	s_lshl_b32 s12, s97, 8
	s_add_u32 s12, s92, s12
	s_addc_u32 s13, s93, 0
	v_mov_b32_e32 v0, 0x5400
	v_mov_b32_e32 v1, 1
	global_atomic_add v2, v0, v1, s[12:13] sc0
	s_add_i32 s17, s98, 1
	s_mul_i32 s18, s17, s14
	s_mul_i32 s19, s17, s15
	s_lshl_b32 s21, s97, 2
	s_add_i32 s21, s21, 0x7540
	s_waitcnt vmcnt(0)
	buffer_inv sc1
	v_readfirstlane_b32 s16, v2
	s_add_i32 s16, s16, 1
	s_cmp_lg_u32 s16, s18
	s_cbranch_scc1 .Lxb_poll_0
	buffer_wbl2 sc1
	s_waitcnt vmcnt(0)
	v_mov_b32_e32 v0, s21
	global_atomic_add v0, v1, s[92:93]
.Lxb_poll_0:
	v_mov_b32_e32 v0, 0x7540
	s_mov_b32 s20, 0
.Lxb_loop_0:
	global_load_dwordx4 v[2:5], v0, s[92:93] sc1
	global_load_dwordx4 v[6:9], v0, s[92:93] offset:16 sc1
	global_load_dwordx4 v[10:13], v0, s[92:93] offset:32 sc1
	global_load_dwordx4 v[14:17], v0, s[92:93] offset:48 sc1
	s_waitcnt vmcnt(0)
	v_add3_u32 v2, v2, v3, v4
	v_add3_u32 v5, v5, v6, v7
	v_add3_u32 v8, v8, v9, v10
	v_add3_u32 v11, v11, v12, v13
	v_add3_u32 v14, v14, v15, v16
	v_add3_u32 v2, v2, v5, v8
	v_add3_u32 v2, v2, v11, v14
	v_add_u32_e32 v2, v2, v17
	s_nop 1
	v_readfirstlane_b32 s21, v2
	s_cmp_ge_u32 s21, s19
	s_cbranch_scc1 .Lxb_done_0
	s_sleep 1
	s_add_i32 s20, s20, 1
	s_and_b32 s17, s20, 0xff
	s_cmp_lg_u32 s17, 0
	s_cbranch_scc1 .Lxb_loop_0
	v_mov_b32_e32 v1, 0x4200
	global_load_dword v1, v1, s[92:93] sc1
	s_waitcnt vmcnt(0)
	v_readfirstlane_b32 s17, v1
	s_cmp_lg_u32 s17, 0
	s_cbranch_scc1 .Lxb_done_0
	s_cmp_lt_u32 s20, 0x40001
	s_cbranch_scc1 .Lxb_loop_0
	v_mov_b32_e32 v1, 0x4200
	v_mov_b32_e32 v3, 1
	global_atomic_add v1, v3, s[92:93]
.Lxb_done_0:
	s_add_i32 s98, s98, 1
	s_waitcnt vmcnt(0)

; __device__ __forceinline__ int tid_from_wave(int wave) { unsigned l_; asm volatile("v_mbcnt_lo_u32_b32 %0, -1, 0\n\tv_mbcnt_hi_u32_b32 %0, -1, %0" : "=v"(l_)); return wave * 64 + (int)l_; }
; __device__ __forceinline__ unsigned xb_ld(unsigned* p)              { return __hip_atomic_load(p, __ATOMIC_RELAXED, __HIP_MEMORY_SCOPE_AGENT); }
; __device__ __forceinline__ unsigned xb_add(unsigned* p, unsigned v) { return __hip_atomic_fetch_add(p, v, __ATOMIC_RELAXED, __HIP_MEMORY_SCOPE_AGENT); }
; #define XB_SPIN(cond, bar) do { unsigned _sp = 0; while (cond) { __builtin_amdgcn_s_sleep(1); \
;     if ((++_sp & 255u) == 0u) { if (xb_ld(&(bar)[XB_TMO])) break; if (_sp > XB_SPIN_CAP) { atomicAdd(&(bar)[XB_TMO], 1u); break; } } } } while (0)
; __device__ __forceinline__ void xcd_barrier(const XcdBarrier& b) {
;     asm volatile("s_waitcnt vmcnt(0)" ::: "memory");
;     __syncthreads();
;     if (tid_from_wave(b.wave) == 0) {
;         unsigned* bar = b.bar;
;         __builtin_amdgcn_s_waitcnt(0);
;         unsigned nloc = b.st[0], nx = b.st[1];
;         if (nloc == 0u) { xcd_barrier_complete(bar, b.x, nloc, nx); b.st[0] = nloc; b.st[1] = nx; }
;         const unsigned old = xb_add(&bar[XB_XSUB(b.x)], 1u);
;         const unsigned gen = old / nloc;
;         if (old + 1u == (gen + 1u) * nloc) {
;             __builtin_amdgcn_fence(__ATOMIC_RELEASE, "agent");
;             asm volatile("s_waitcnt vmcnt(0)" ::: "memory");
;             const unsigned og = xb_add(&bar[XB_TOP], 1u);
;             const unsigned tg = og / nx;
;             if (og + 1u == (tg + 1u) * nx) xb_add(&bar[XB_TOPGEN], 1u);
;             else XB_SPIN(xb_ld(&bar[XB_TOPGEN]) == tg, bar);
;             __builtin_amdgcn_fence(__ATOMIC_ACQUIRE, "agent");
;             xb_add(&bar[XB_XGEN(b.x)], 1u);
;             asm volatile("s_waitcnt vmcnt(0)" ::: "memory");
;         } else {
;             XB_SPIN(xb_ld(&bar[XB_XGEN(b.x)]) == gen, bar);
;             __builtin_amdgcn_fence(__ATOMIC_ACQUIRE, "agent");
;             asm volatile("s_waitcnt vmcnt(0)" ::: "memory");
;         }
;     }
;     __syncthreads();
; }
.Lxb_done_16:
	s_add_i32 s98, s98, 1
	s_waitcnt vmcnt(0)
	s_branch .LBB0_1604

; __device__ __forceinline__ unsigned xb_ld(unsigned* p)              { return __hip_atomic_load(p, __ATOMIC_RELAXED, __HIP_MEMORY_SCOPE_AGENT); }
; __device__ __forceinline__ unsigned xb_add(unsigned* p, unsigned v) { return __hip_atomic_fetch_add(p, v, __ATOMIC_RELAXED, __HIP_MEMORY_SCOPE_AGENT); }
; #define XB_SPIN(cond, bar) do { unsigned _sp = 0; while (cond) { __builtin_amdgcn_s_sleep(1); \
;     if ((++_sp & 255u) == 0u) { if (xb_ld(&(bar)[XB_TMO])) break; if (_sp > XB_SPIN_CAP) { atomicAdd(&(bar)[XB_TMO], 1u); break; } } } } while (0)
; __device__ __forceinline__ void xcd_barrier(const XcdBarrier& b) {
;     ...
;             else XB_SPIN(xb_ld(&bar[XB_TOPGEN]) == tg, bar);
;             __builtin_amdgcn_fence(__ATOMIC_ACQUIRE, "agent");
;             xb_add(&bar[XB_XGEN(b.x)], 1u);
;             asm volatile("s_waitcnt vmcnt(0)" ::: "memory");
;         } else {
;             XB_SPIN(xb_ld(&bar[XB_XGEN(b.x)]) == gen, bar);
;             __builtin_amdgcn_fence(__ATOMIC_ACQUIRE, "agent");
;             asm volatile("s_waitcnt vmcnt(0)" ::: "memory");
;         }
;     }
;     __syncthreads();
.LBB0_1596:
	s_cbranch_execnz .LBB0_1519
	s_branch .LBB0_1547
.LBB0_1604:
	s_or_b64 exec, exec, s[0:1]
	s_waitcnt lgkmcnt(0)
	s_barrier
